# speedup vs baseline: 1.0071x; 1.0071x over previous
.LBB5_6:
	v_ashrrev_i32_e32 v236, 2, v0
	v_and_b32_e32 v237, 0xffffffe0, v236
	v_lshrrev_b32_e32 v236, 2, v0
	v_add_u32_e32 v237, s29, v237
	v_and_b32_e32 v236, 12, v236
	v_or_b32_e32 v238, v237, v236
	v_mov_b32_e32 v236, v238
	v_min_i32_e32 v236, 0x2edc, v236
	v_ashrrev_i32_e32 v237, 31, v236
	v_lshl_add_u64 v[236:237], v[236:237], 2, s[10:11]
	global_load_dwordx4 v[240:243], v[236:237], off
	v_or_b32_e32 v236, 16, v238
	v_min_i32_e32 v236, 0x2edc, v236
	v_ashrrev_i32_e32 v237, 31, v236
	v_lshl_add_u64 v[236:237], v[236:237], 2, s[10:11]
	global_load_dwordx4 v[244:247], v[236:237], off
	v_add_u32_e32 v236, 0x80, v238
	v_min_i32_e32 v236, 0x2edc, v236
	v_ashrrev_i32_e32 v237, 31, v236
	v_lshl_add_u64 v[236:237], v[236:237], 2, s[10:11]
	global_load_dwordx4 v[248:251], v[236:237], off
	v_add_u32_e32 v236, 0x90, v238
	v_min_i32_e32 v236, 0x2edc, v236
	v_ashrrev_i32_e32 v237, 31, v236
	v_lshl_add_u64 v[236:237], v[236:237], 2, s[10:11]
	global_load_dwordx4 v[252:255], v[236:237], off
	s_or_b32 s30, s29, 0x80
	s_lshl_b32 s0, s30, 11
	v_readfirstlane_b32 s6, v130
	s_or_b32 s1, s0, 0x80
	s_mov_b32 m0, s6
	v_readfirstlane_b32 s6, v131
	ds_read_b128 v[2:5], v132
	ds_read_b128 v[6:9], v132 offset:1024
	ds_read_b128 v[10:13], v133
	ds_read_b128 v[14:17], v133 offset:1024
	ds_read_b128 v[18:21], v134
	ds_read_b128 v[22:25], v134 offset:1024
	buffer_load_dwordx4 v1, s[12:15], s1 offen lds
	s_mov_b32 m0, s6
	s_mov_b32 s31, s33
	buffer_load_dwordx4 v114, s[12:15], s1 offen lds
	ds_read_b128 v[26:29], v135
	ds_read_b128 v[30:33], v135 offset:1024
	ds_read_b128 v[34:37], v136
	ds_read_b128 v[38:41], v136 offset:1024
	ds_read_b128 v[42:45], v137
	ds_read_b128 v[46:49], v137 offset:1024
	ds_read_b128 v[50:53], v138
	ds_read_b128 v[54:57], v138 offset:1024
	ds_read_b128 v[58:61], v138 offset:2048
	ds_read_b128 v[62:65], v139 offset:3072
	s_waitcnt lgkmcnt(0)
	s_barrier
	s_setprio 1
	s_waitcnt lgkmcnt(3)
	v_mfma_f32_16x16x32_f16 v[66:69], v[50:53], v[2:5], 0
	v_mfma_f32_16x16x32_f16 v[70:73], v[50:53], v[10:13], 0
	v_mfma_f32_16x16x32_f16 v[74:77], v[50:53], v[18:21], 0
	s_waitcnt lgkmcnt(1)
	v_mfma_f32_16x16x32_f16 v[78:81], v[58:61], v[2:5], 0
	v_mfma_f32_16x16x32_f16 v[82:85], v[58:61], v[10:13], 0
	v_mfma_f32_16x16x32_f16 v[86:89], v[58:61], v[18:21], 0
	v_mfma_f32_16x16x32_f16 v[66:69], v[54:57], v[6:9], v[66:69]
	v_mfma_f32_16x16x32_f16 v[70:73], v[54:57], v[14:17], v[70:73]
	v_mfma_f32_16x16x32_f16 v[74:77], v[54:57], v[22:25], v[74:77]
	s_waitcnt lgkmcnt(0)
	v_mfma_f32_16x16x32_f16 v[78:81], v[62:65], v[6:9], v[78:81]
	v_mfma_f32_16x16x32_f16 v[82:85], v[62:65], v[14:17], v[82:85]
	v_mfma_f32_16x16x32_f16 v[86:89], v[62:65], v[22:25], v[86:89]
	s_setprio 0
	s_setprio 1
	v_mfma_f32_16x16x32_f16 v[90:93], v[50:53], v[26:29], 0
	v_mfma_f32_16x16x32_f16 v[94:97], v[50:53], v[34:37], 0
	v_mfma_f32_16x16x32_f16 v[50:53], v[50:53], v[42:45], 0
	v_mfma_f32_16x16x32_f16 v[90:93], v[54:57], v[30:33], v[90:93]
	v_mfma_f32_16x16x32_f16 v[94:97], v[54:57], v[38:41], v[94:97]
	v_mfma_f32_16x16x32_f16 v[50:53], v[54:57], v[46:49], v[50:53]
	v_mfma_f32_16x16x32_f16 v[54:57], v[58:61], v[26:29], 0
	v_mfma_f32_16x16x32_f16 v[98:101], v[58:61], v[34:37], 0
	v_mfma_f32_16x16x32_f16 v[58:61], v[58:61], v[42:45], 0
	v_mfma_f32_16x16x32_f16 v[54:57], v[62:65], v[30:33], v[54:57]
	v_mfma_f32_16x16x32_f16 v[58:61], v[62:65], v[46:49], v[58:61]
	v_mfma_f32_16x16x32_f16 v[98:101], v[62:65], v[38:41], v[98:101]
	s_setprio 0
	s_barrier
	s_lshl_b32 s1, s33, 11
	v_readfirstlane_b32 s7, v115
	s_or_b32 s6, s1, 0x100
	s_mov_b32 m0, s7
	v_readfirstlane_b32 s7, v117
	ds_read_b128 v[62:65], v138 offset:16384
	ds_read_b128 v[102:105], v138 offset:17408
	ds_read_b128 v[106:109], v138 offset:18432
	ds_read_b128 v[110:113], v139 offset:19456
	buffer_load_dwordx4 v1, s[16:19], s6 offen lds
	s_mov_b32 m0, s7
	v_readfirstlane_b32 s7, v120
	buffer_load_dwordx4 v116, s[16:19], s6 offen lds
	s_add_i32 s6, s1, 0x30100
	s_mov_b32 m0, s7
	v_readfirstlane_b32 s7, v121
	buffer_load_dwordx4 v1, s[16:19], s6 offen lds
	s_mov_b32 m0, s7
	v_readfirstlane_b32 s33, v118
	buffer_load_dwordx4 v116, s[16:19], s6 offen lds
	s_lshl_b32 s6, s29, 11
	s_or_b32 s7, s6, 0x100
	s_mov_b32 m0, s33
	v_readfirstlane_b32 s33, v119
	buffer_load_dwordx4 v1, s[12:15], s7 offen lds
	s_mov_b32 m0, s33
	s_nop 0
	buffer_load_dwordx4 v114, s[12:15], s7 offen lds
	s_waitcnt lgkmcnt(0)
	s_barrier
	s_setprio 1
	s_waitcnt lgkmcnt(3)
	v_mfma_f32_16x16x32_f16 v[146:149], v[62:65], v[2:5], 0
	s_waitcnt lgkmcnt(1)
	v_mfma_f32_16x16x32_f16 v[2:5], v[106:109], v[2:5], 0
	s_waitcnt lgkmcnt(0)
	v_mfma_f32_16x16x32_f16 v[158:161], v[110:113], v[6:9], v[2:5]
	v_mfma_f32_16x16x32_f16 v[2:5], v[106:109], v[10:13], 0
	v_mfma_f32_16x16x32_f16 v[150:153], v[62:65], v[10:13], 0
	v_mfma_f32_16x16x32_f16 v[154:157], v[62:65], v[18:21], 0
	v_mfma_f32_16x16x32_f16 v[162:165], v[110:113], v[14:17], v[2:5]
	v_mfma_f32_16x16x32_f16 v[2:5], v[106:109], v[18:21], 0
	v_mfma_f32_16x16x32_f16 v[146:149], v[102:105], v[6:9], v[146:149]
	v_mfma_f32_16x16x32_f16 v[150:153], v[102:105], v[14:17], v[150:153]
	v_mfma_f32_16x16x32_f16 v[154:157], v[102:105], v[22:25], v[154:157]
	v_mfma_f32_16x16x32_f16 v[166:169], v[110:113], v[22:25], v[2:5]
	s_setprio 0
	s_setprio 1
	v_mfma_f32_16x16x32_f16 v[2:5], v[62:65], v[26:29], 0
	v_mfma_f32_16x16x32_f16 v[170:173], v[102:105], v[30:33], v[2:5]
	v_mfma_f32_16x16x32_f16 v[2:5], v[62:65], v[34:37], 0
	v_mfma_f32_16x16x32_f16 v[174:177], v[102:105], v[38:41], v[2:5]
	v_mfma_f32_16x16x32_f16 v[2:5], v[62:65], v[42:45], 0
	v_mfma_f32_16x16x32_f16 v[62:65], v[102:105], v[46:49], v[2:5]
	v_mfma_f32_16x16x32_f16 v[2:5], v[106:109], v[26:29], 0
	v_mfma_f32_16x16x32_f16 v[102:105], v[110:113], v[30:33], v[2:5]
	v_mfma_f32_16x16x32_f16 v[2:5], v[106:109], v[34:37], 0
	v_mfma_f32_16x16x32_f16 v[178:181], v[110:113], v[38:41], v[2:5]
	v_mfma_f32_16x16x32_f16 v[2:5], v[106:109], v[42:45], 0
	v_mfma_f32_16x16x32_f16 v[106:109], v[110:113], v[46:49], v[2:5]
	s_setprio 0
	s_barrier
	v_readfirstlane_b32 s33, v122
	s_or_b32 s7, s0, 0x100
	s_mov_b32 m0, s33
	v_readfirstlane_b32 s33, v123
	s_nop 0
	ds_read_b128 v[2:5], v138 offset:32768
	ds_read_b128 v[6:9], v138 offset:33792
	ds_read_b128 v[110:113], v138 offset:34816
	ds_read_b128 v[182:185], v139 offset:35840
	buffer_load_dwordx4 v1, s[12:15], s7 offen lds
	s_mov_b32 m0, s33
	s_nop 0
	buffer_load_dwordx4 v114, s[12:15], s7 offen lds
	ds_read_b128 v[186:189], v140
	ds_read_b128 v[190:193], v140 offset:1024
	ds_read_b128 v[194:197], v141
	ds_read_b128 v[198:201], v141 offset:1024
	ds_read_b128 v[202:205], v142
	ds_read_b128 v[206:209], v142 offset:1024
	ds_read_b128 v[210:213], v143
	ds_read_b128 v[214:217], v143 offset:1024
	ds_read_b128 v[218:221], v144
	ds_read_b128 v[222:225], v144 offset:1024
	ds_read_b128 v[226:229], v145
	ds_read_b128 v[230:233], v145 offset:1024
	s_waitcnt vmcnt(8)
	s_waitcnt lgkmcnt(0)
	s_barrier
	s_setprio 1
	s_waitcnt lgkmcnt(11)
	v_mfma_f32_16x16x32_f16 v[10:13], v[2:5], v[186:189], v[66:69]
	s_waitcnt lgkmcnt(10)
	v_mfma_f32_16x16x32_f16 v[46:49], v[6:9], v[190:193], v[10:13]
	s_waitcnt lgkmcnt(9)
	v_mfma_f32_16x16x32_f16 v[10:13], v[2:5], v[194:197], v[70:73]
	s_waitcnt lgkmcnt(8)
	v_mfma_f32_16x16x32_f16 v[42:45], v[6:9], v[198:201], v[10:13]
	s_waitcnt lgkmcnt(7)
	v_mfma_f32_16x16x32_f16 v[10:13], v[2:5], v[202:205], v[74:77]
	s_waitcnt lgkmcnt(6)
	v_mfma_f32_16x16x32_f16 v[38:41], v[6:9], v[206:209], v[10:13]
	v_mfma_f32_16x16x32_f16 v[10:13], v[110:113], v[186:189], v[78:81]
	v_mfma_f32_16x16x32_f16 v[34:37], v[182:185], v[190:193], v[10:13]
	v_mfma_f32_16x16x32_f16 v[10:13], v[110:113], v[194:197], v[82:85]
	v_mfma_f32_16x16x32_f16 v[30:33], v[182:185], v[198:201], v[10:13]
	v_mfma_f32_16x16x32_f16 v[10:13], v[110:113], v[202:205], v[86:89]
	v_mfma_f32_16x16x32_f16 v[26:29], v[182:185], v[206:209], v[10:13]
	s_setprio 0
	s_setprio 1
	s_waitcnt lgkmcnt(5)
	v_mfma_f32_16x16x32_f16 v[10:13], v[2:5], v[210:213], v[90:93]
	s_waitcnt lgkmcnt(4)
	v_mfma_f32_16x16x32_f16 v[22:25], v[6:9], v[214:217], v[10:13]
	s_waitcnt lgkmcnt(3)
	v_mfma_f32_16x16x32_f16 v[10:13], v[2:5], v[218:221], v[94:97]
	s_waitcnt lgkmcnt(1)
	v_mfma_f32_16x16x32_f16 v[2:5], v[2:5], v[226:229], v[50:53]
	s_waitcnt lgkmcnt(0)
	v_mfma_f32_16x16x32_f16 v[14:17], v[6:9], v[230:233], v[2:5]
	v_mfma_f32_16x16x32_f16 v[2:5], v[110:113], v[210:213], v[54:57]
	v_mfma_f32_16x16x32_f16 v[18:21], v[6:9], v[222:225], v[10:13]
	v_mfma_f32_16x16x32_f16 v[10:13], v[182:185], v[214:217], v[2:5]
	v_mfma_f32_16x16x32_f16 v[2:5], v[110:113], v[218:221], v[98:101]
	v_mfma_f32_16x16x32_f16 v[6:9], v[182:185], v[222:225], v[2:5]
	v_mfma_f32_16x16x32_f16 v[2:5], v[110:113], v[226:229], v[58:61]
	v_mfma_f32_16x16x32_f16 v[2:5], v[182:185], v[230:233], v[2:5]
	s_setprio 0
	s_barrier
	v_readfirstlane_b32 s33, v124
	s_or_b32 s7, s1, 0x180
	s_mov_b32 m0, s33
	v_readfirstlane_b32 s33, v125
	ds_read_b128 v[50:53], v138 offset:49152
	ds_read_b128 v[54:57], v138 offset:50176
	ds_read_b128 v[98:101], v138 offset:51200
	ds_read_b128 v[110:113], v139 offset:52224
	buffer_load_dwordx4 v1, s[16:19], s7 offen lds
	s_mov_b32 m0, s33
	v_readfirstlane_b32 s33, v128
	buffer_load_dwordx4 v116, s[16:19], s7 offen lds
	s_add_i32 s7, s1, 0x30180
	s_mov_b32 m0, s33
	v_readfirstlane_b32 s33, v129
	buffer_load_dwordx4 v1, s[16:19], s7 offen lds
	s_mov_b32 m0, s33
	v_readfirstlane_b32 s33, v126
	buffer_load_dwordx4 v116, s[16:19], s7 offen lds
	s_or_b32 s7, s6, 0x180
	s_mov_b32 m0, s33
	v_readfirstlane_b32 s33, v127
	buffer_load_dwordx4 v1, s[12:15], s7 offen lds
	s_mov_b32 m0, s33
	s_nop 0
	buffer_load_dwordx4 v114, s[12:15], s7 offen lds
	s_waitcnt vmcnt(8)
	s_waitcnt lgkmcnt(0)
	s_barrier
	s_setprio 1
	s_waitcnt lgkmcnt(3)
	v_mfma_f32_16x16x32_f16 v[58:61], v[50:53], v[186:189], v[146:149]
	s_waitcnt lgkmcnt(2)
	v_mfma_f32_16x16x32_f16 v[94:97], v[54:57], v[190:193], v[58:61]
	v_mfma_f32_16x16x32_f16 v[58:61], v[50:53], v[194:197], v[150:153]
	v_mfma_f32_16x16x32_f16 v[90:93], v[54:57], v[198:201], v[58:61]
	v_mfma_f32_16x16x32_f16 v[58:61], v[50:53], v[202:205], v[154:157]
	v_mfma_f32_16x16x32_f16 v[86:89], v[54:57], v[206:209], v[58:61]
	s_waitcnt lgkmcnt(1)
	v_mfma_f32_16x16x32_f16 v[58:61], v[98:101], v[186:189], v[158:161]
	s_waitcnt lgkmcnt(0)
	v_mfma_f32_16x16x32_f16 v[82:85], v[110:113], v[190:193], v[58:61]
	v_mfma_f32_16x16x32_f16 v[58:61], v[98:101], v[194:197], v[162:165]
	v_mfma_f32_16x16x32_f16 v[78:81], v[110:113], v[198:201], v[58:61]
	v_mfma_f32_16x16x32_f16 v[58:61], v[98:101], v[202:205], v[166:169]
	v_mfma_f32_16x16x32_f16 v[74:77], v[110:113], v[206:209], v[58:61]
	s_setprio 0
	s_setprio 1
	v_mfma_f32_16x16x32_f16 v[58:61], v[50:53], v[210:213], v[170:173]
	v_mfma_f32_16x16x32_f16 v[70:73], v[54:57], v[214:217], v[58:61]
	v_mfma_f32_16x16x32_f16 v[58:61], v[50:53], v[218:221], v[174:177]
	v_mfma_f32_16x16x32_f16 v[50:53], v[50:53], v[226:229], v[62:65]
	v_mfma_f32_16x16x32_f16 v[62:65], v[54:57], v[230:233], v[50:53]
	v_mfma_f32_16x16x32_f16 v[50:53], v[98:101], v[210:213], v[102:105]
	v_mfma_f32_16x16x32_f16 v[66:69], v[54:57], v[222:225], v[58:61]
	v_mfma_f32_16x16x32_f16 v[58:61], v[110:113], v[214:217], v[50:53]
	v_mfma_f32_16x16x32_f16 v[50:53], v[98:101], v[218:221], v[178:181]
	v_mfma_f32_16x16x32_f16 v[54:57], v[110:113], v[222:225], v[50:53]
	v_mfma_f32_16x16x32_f16 v[50:53], v[98:101], v[226:229], v[106:109]
	v_mfma_f32_16x16x32_f16 v[50:53], v[110:113], v[230:233], v[50:53]
	s_setprio 0
	s_barrier
	s_mov_b32 s7, 0
	s_mov_b32 s33, 0

.LBB5_10:
	s_or_b64 exec, exec, s[0:1]
	v_mov_b32_e32 v147, v0
	s_add_i32 s24, s24, s27
	v_ashrrev_i32_e32 v50, 2, v147
	v_and_b32_e32 v146, 0xffffffe0, v50
	v_lshrrev_b32_e32 v50, 2, v147
	v_add_u32_e32 v151, s29, v146
	v_and_b32_e32 v148, 12, v50
	v_or_b32_e32 v54, v151, v148
	v_or_b32_e32 v52, 16, v54
	v_min_i32_e32 v50, 0x2edc, v54
	v_min_i32_e32 v52, 0x2edc, v52
	v_ashrrev_i32_e32 v51, 31, v50
	v_ashrrev_i32_e32 v53, 31, v52
	v_lshl_add_u64 v[50:51], v[50:51], 2, s[10:11]
	v_lshl_add_u64 v[52:53], v[52:53], 2, s[10:11]
	v_mov_b32_e32 v110, v240
	v_mov_b32_e32 v111, v241
	v_mov_b32_e32 v112, v242
	v_mov_b32_e32 v113, v243
	v_mov_b32_e32 v106, v244
	v_mov_b32_e32 v107, v245
	v_mov_b32_e32 v108, v246
	v_mov_b32_e32 v109, v247
	v_add_u32_e32 v50, 0x80, v54
	v_add_u32_e32 v52, 0x90, v54
	v_min_i32_e32 v50, 0x2edc, v50
	v_min_i32_e32 v52, 0x2edc, v52
	v_ashrrev_i32_e32 v51, 31, v50
	v_ashrrev_i32_e32 v53, 31, v52
	v_lshl_add_u64 v[50:51], v[50:51], 2, s[10:11]
	v_lshl_add_u64 v[52:53], v[52:53], 2, s[10:11]
	v_mov_b32_e32 v54, v248
	v_mov_b32_e32 v55, v249
	v_mov_b32_e32 v56, v250
	v_mov_b32_e32 v57, v251
	s_nop 0
	v_mov_b32_e32 v50, v252
	v_mov_b32_e32 v51, v253
	v_mov_b32_e32 v52, v254
	v_mov_b32_e32 v53, v255
	s_cmpk_lt_u32 s24, 0x5e
	s_cselect_b64 s[0:1], -1, 0
	s_cmpk_gt_u32 s24, 0x5d
	s_mov_b32 s33, s31
	s_waitcnt vmcnt(0)
	s_cbranch_scc1 .LBB5_12
	s_add_i32 s6, s24, s25
	s_lshr_b32 s7, s6, 4
	s_and_b32 s29, s7, 0x78
	s_sub_i32 s7, 47, s29
	s_min_u32 s33, s7, 8
	v_cvt_f32_ubyte0_e32 v149, s33
	v_rcp_iflag_f32_e32 v150, v149
	s_and_b32 s34, s6, 0x7f
	v_cvt_f32_ubyte0_e32 v152, s34
	v_readfirstlane_b32 s35, v120
	v_mul_f32_e32 v150, v152, v150
	v_trunc_f32_e32 v150, v150
	v_cvt_u32_f32_e32 v153, v150
	v_fma_f32 v150, -v150, v149, v152
	v_cmp_ge_f32_e64 s[6:7], |v150|, v149
	s_cmp_lg_u64 s[6:7], 0
	v_readfirstlane_b32 s6, v153
	s_addc_u32 s6, s6, 0
	s_mul_i32 s7, s6, s33
	s_sub_i32 s7, s34, s7
	s_and_b32 s6, s6, 0xff
	s_and_b32 s7, s7, 0xff
	v_readfirstlane_b32 s33, v115
	s_add_i32 s29, s29, s7
	s_mul_i32 s7, s6, 0x60000
	s_mov_b32 m0, s33
	v_readfirstlane_b32 s33, v117
	buffer_load_dwordx4 v1, s[16:19], s7 offen lds
	s_mov_b32 m0, s33
	v_readfirstlane_b32 s34, v118
	buffer_load_dwordx4 v116, s[16:19], s7 offen lds
	s_lshl_b32 s33, s29, 19
	s_mov_b32 m0, s34
	v_readfirstlane_b32 s34, v119
	buffer_load_dwordx4 v1, s[12:15], s33 offen lds
	s_mov_b32 m0, s34
	s_add_i32 s34, s7, 0x30000
	buffer_load_dwordx4 v114, s[12:15], s33 offen lds
	s_mov_b32 m0, s35
	v_readfirstlane_b32 s35, v121
	buffer_load_dwordx4 v1, s[16:19], s34 offen lds
	s_mov_b32 m0, s35
	v_readfirstlane_b32 s35, v122
	buffer_load_dwordx4 v116, s[16:19], s34 offen lds
	s_or_b32 s34, s33, 0x40000
	s_mov_b32 m0, s35
	v_readfirstlane_b32 s35, v123
	buffer_load_dwordx4 v1, s[12:15], s34 offen lds
	s_mov_b32 m0, s35
	v_readfirstlane_b32 s35, v124
	buffer_load_dwordx4 v114, s[12:15], s34 offen lds
	s_or_b32 s34, s7, 0x80
	s_mov_b32 m0, s35
	v_readfirstlane_b32 s35, v125
	buffer_load_dwordx4 v1, s[16:19], s34 offen lds
	s_mov_b32 m0, s35
	s_bitset1_b32 s33, 7
	buffer_load_dwordx4 v116, s[16:19], s34 offen lds
	v_readfirstlane_b32 s34, v126
	s_mov_b32 m0, s34
	v_readfirstlane_b32 s34, v127
	buffer_load_dwordx4 v1, s[12:15], s33 offen lds
	s_mov_b32 m0, s34
	s_add_i32 s7, s7, 0x30080
	buffer_load_dwordx4 v114, s[12:15], s33 offen lds
	v_readfirstlane_b32 s33, v128
	s_mov_b32 m0, s33
	v_readfirstlane_b32 s33, v129
	buffer_load_dwordx4 v1, s[16:19], s7 offen lds
	s_mov_b32 m0, s33
	s_lshl_b32 s29, s29, 8
	buffer_load_dwordx4 v116, s[16:19], s7 offen lds
	s_mul_i32 s33, s6, 0xc0

	.amdhsa_kernel _Z11gemm_8phaseILi1EEvPKDF16_S1_PfPKfS4_
		.amdhsa_group_segment_fixed_size 0
		.amdhsa_private_segment_fixed_size 0
		.amdhsa_kernarg_size 296
		.amdhsa_user_sgpr_count 2
		.amdhsa_user_sgpr_dispatch_ptr 0
		.amdhsa_user_sgpr_queue_ptr 0
		.amdhsa_user_sgpr_kernarg_segment_ptr 1
		.amdhsa_user_sgpr_dispatch_id 0
		.amdhsa_user_sgpr_kernarg_preload_length 0
		.amdhsa_user_sgpr_kernarg_preload_offset 0
		.amdhsa_user_sgpr_private_segment_size 0
		.amdhsa_uses_dynamic_stack 0
		.amdhsa_enable_private_segment 0
		.amdhsa_system_sgpr_workgroup_id_x 1
		.amdhsa_system_sgpr_workgroup_id_y 0
		.amdhsa_system_sgpr_workgroup_id_z 0
		.amdhsa_system_sgpr_workgroup_info 0
		.amdhsa_system_vgpr_workitem_id 0
		.amdhsa_next_free_vgpr 256
		.amdhsa_next_free_sgpr 38
		.amdhsa_accum_offset 256
		.amdhsa_reserve_vcc 1
		.amdhsa_float_round_mode_32 0
		.amdhsa_float_round_mode_16_64 0
		.amdhsa_float_denorm_mode_32 3
		.amdhsa_float_denorm_mode_16_64 3
		.amdhsa_dx10_clamp 1
		.amdhsa_ieee_mode 1
		.amdhsa_fp16_overflow 0
		.amdhsa_tg_split 0
		.amdhsa_exception_fp_ieee_invalid_op 0
		.amdhsa_exception_fp_denorm_src 0
		.amdhsa_exception_fp_ieee_div_zero 0
		.amdhsa_exception_fp_ieee_overflow 0
		.amdhsa_exception_fp_ieee_underflow 0
		.amdhsa_exception_fp_ieee_inexact 0
		.amdhsa_exception_int_div_zero 0
	.end_amdhsa_kernel

amdhsa.kernels:
  - .agpr_count:     0
    .args:
      - .actual_access:  read_only
        .address_space:  global
        .offset:         0
        .size:           8
        .value_kind:     global_buffer
      - .actual_access:  read_only
        .address_space:  global
        .offset:         8
        .size:           8
        .value_kind:     global_buffer
      - .actual_access:  read_only
        .address_space:  global
        .offset:         16
        .size:           8
        .value_kind:     global_buffer
      - .actual_access:  read_only
        .address_space:  global
        .offset:         24
        .size:           8
        .value_kind:     global_buffer
      - .actual_access:  read_only
        .address_space:  global
        .offset:         32
        .size:           8
        .value_kind:     global_buffer
      - .actual_access:  read_only
        .address_space:  global
        .offset:         40
        .size:           8
        .value_kind:     global_buffer
      - .address_space:  global
        .offset:         48
        .size:           8
        .value_kind:     global_buffer
      - .address_space:  global
        .offset:         56
        .size:           8
        .value_kind:     global_buffer
      - .address_space:  global
        .offset:         64
        .size:           8
        .value_kind:     global_buffer
      - .address_space:  global
        .offset:         72
        .size:           8
        .value_kind:     global_buffer
      - .address_space:  global
        .offset:         80
        .size:           8
        .value_kind:     global_buffer
    .group_segment_fixed_size: 0
    .kernarg_segment_align: 8
    .kernarg_segment_size: 88
    .language:       OpenCL C
    .language_version:
      - 2
      - 0
    .max_flat_workgroup_size: 256
    .name:           _Z11prep_kernelPKfPKiS0_S0_S0_S0_PDF16_S3_S3_S3_Pc
    .private_segment_fixed_size: 0
    .sgpr_count:     33
    .sgpr_spill_count: 0
    .symbol:         _Z11prep_kernelPKfPKiS0_S0_S0_S0_PDF16_S3_S3_S3_Pc.kd
    .uniform_work_group_size: 1
    .uses_dynamic_stack: false
    .vgpr_count:     14
    .vgpr_spill_count: 0
    .wavefront_size: 64
  - .agpr_count:     0
    .args:
      - .actual_access:  read_only
        .address_space:  global
        .offset:         0
        .size:           8
        .value_kind:     global_buffer
      - .address_space:  global
        .offset:         8
        .size:           8
        .value_kind:     global_buffer
    .group_segment_fixed_size: 0
    .kernarg_segment_align: 8
    .kernarg_segment_size: 16
    .language:       OpenCL C
    .language_version:
      - 2
      - 0
    .max_flat_workgroup_size: 256
    .name:           _Z7cvt_wfcPKfPDF16_
    .private_segment_fixed_size: 0
    .sgpr_count:     12
    .sgpr_spill_count: 0
    .symbol:         _Z7cvt_wfcPKfPDF16_.kd
    .uniform_work_group_size: 1
    .uses_dynamic_stack: false
    .vgpr_count:     12
    .vgpr_spill_count: 0
    .wavefront_size: 64
  - .agpr_count:     12
    .args:
      - .actual_access:  read_only
        .address_space:  global
        .offset:         0
        .size:           8
        .value_kind:     global_buffer
      - .actual_access:  read_only
        .address_space:  global
        .offset:         8
        .size:           8
        .value_kind:     global_buffer
      - .address_space:  global
        .offset:         16
        .size:           8
        .value_kind:     global_buffer
      - .address_space:  global
        .offset:         24
        .size:           8
        .value_kind:     global_buffer
      - .offset:         32
        .size:           4
        .value_kind:     by_value
    .group_segment_fixed_size: 0
    .kernarg_segment_align: 8
    .kernarg_segment_size: 36
    .language:       OpenCL C
    .language_version:
      - 2
      - 0
    .max_flat_workgroup_size: 256
    .name:           _Z9lstm_stepPKfS0_PDF16_Pfi
    .private_segment_fixed_size: 0
    .sgpr_count:     21
    .sgpr_spill_count: 0
    .symbol:         _Z9lstm_stepPKfS0_PDF16_Pfi.kd
    .uniform_work_group_size: 1
    .uses_dynamic_stack: false
    .vgpr_count:     88
    .vgpr_spill_count: 0
    .wavefront_size: 64
  - .agpr_count:     0
    .args:
      - .actual_access:  read_only
        .address_space:  global
        .offset:         0
        .size:           8
        .value_kind:     global_buffer
      - .actual_access:  read_only
        .address_space:  global
        .offset:         8
        .size:           8
        .value_kind:     global_buffer
      - .address_space:  global
        .offset:         16
        .size:           8
        .value_kind:     global_buffer
      - .address_space:  global
        .offset:         24
        .size:           8
        .value_kind:     global_buffer
      - .address_space:  global
        .offset:         32
        .size:           8
        .value_kind:     global_buffer
      - .actual_access:  read_only
        .address_space:  global
        .offset:         40
        .size:           8
        .value_kind:     global_buffer
      - .address_space:  global
        .offset:         48
        .size:           8
        .value_kind:     global_buffer
    .group_segment_fixed_size: 0
    .kernarg_segment_align: 8
    .kernarg_segment_size: 56
    .language:       OpenCL C
    .language_version:
      - 2
      - 0
    .max_flat_workgroup_size: 512
    .name:           _Z15lstm_persistentPKDF16_PKfPDF16_PjS4_S2_S3_
    .private_segment_fixed_size: 0
    .sgpr_count:     62
    .sgpr_spill_count: 0
    .symbol:         _Z15lstm_persistentPKDF16_PKfPDF16_PjS4_S2_S3_.kd
    .uniform_work_group_size: 1
    .uses_dynamic_stack: false
    .vgpr_count:     242
    .vgpr_spill_count: 0
    .wavefront_size: 64
  - .agpr_count:     0
    .args:
      - .address_space:  global
        .offset:         0
        .size:           8
        .value_kind:     global_buffer
      - .address_space:  global
        .offset:         8
        .size:           8
        .value_kind:     global_buffer
      - .address_space:  global
        .offset:         16
        .size:           8
        .value_kind:     global_buffer
      - .address_space:  global
        .offset:         24
        .size:           8
        .value_kind:     global_buffer
      - .address_space:  global
        .offset:         32
        .size:           8
        .value_kind:     global_buffer
      - .offset:         40
        .size:           4
        .value_kind:     hidden_block_count_x
      - .offset:         44
        .size:           4
        .value_kind:     hidden_block_count_y
      - .offset:         48
        .size:           4
        .value_kind:     hidden_block_count_z
      - .offset:         52
        .size:           2
        .value_kind:     hidden_group_size_x
      - .offset:         54
        .size:           2
        .value_kind:     hidden_group_size_y
      - .offset:         56
        .size:           2
        .value_kind:     hidden_group_size_z
      - .offset:         58
        .size:           2
        .value_kind:     hidden_remainder_x
      - .offset:         60
        .size:           2
        .value_kind:     hidden_remainder_y
      - .offset:         62
        .size:           2
        .value_kind:     hidden_remainder_z
      - .offset:         80
        .size:           8
        .value_kind:     hidden_global_offset_x
      - .offset:         88
        .size:           8
        .value_kind:     hidden_global_offset_y
      - .offset:         96
        .size:           8
        .value_kind:     hidden_global_offset_z
      - .offset:         104
        .size:           2
        .value_kind:     hidden_grid_dims
      - .offset:         160
        .size:           4
        .value_kind:     hidden_dynamic_lds_size
    .group_segment_fixed_size: 0
    .kernarg_segment_align: 8
    .kernarg_segment_size: 296
    .language:       OpenCL C
    .language_version:
      - 2
      - 0
    .max_flat_workgroup_size: 512
    .name:           _Z11gemm_8phaseILi0EEvPKDF16_S1_PfPKfS4_
    .private_segment_fixed_size: 0
    .sgpr_count:     59
    .sgpr_spill_count: 0
    .symbol:         _Z11gemm_8phaseILi0EEvPKDF16_S1_PfPKfS4_.kd
    .uniform_work_group_size: 1
    .uses_dynamic_stack: false
    .vgpr_count:     226
    .vgpr_spill_count: 0
    .wavefront_size: 64
  - .agpr_count:     0
    .args:
      - .address_space:  global
        .offset:         0
        .size:           8
        .value_kind:     global_buffer
      - .address_space:  global
        .offset:         8
        .size:           8
        .value_kind:     global_buffer
      - .address_space:  global
        .offset:         16
        .size:           8
        .value_kind:     global_buffer
      - .address_space:  global
        .offset:         24
        .size:           8
        .value_kind:     global_buffer
      - .address_space:  global
        .offset:         32
        .size:           8
        .value_kind:     global_buffer
      - .offset:         40
        .size:           4
        .value_kind:     hidden_block_count_x
      - .offset:         44
        .size:           4
        .value_kind:     hidden_block_count_y
      - .offset:         48
        .size:           4
        .value_kind:     hidden_block_count_z
      - .offset:         52
        .size:           2
        .value_kind:     hidden_group_size_x
      - .offset:         54
        .size:           2
        .value_kind:     hidden_group_size_y
      - .offset:         56
        .size:           2
        .value_kind:     hidden_group_size_z
      - .offset:         58
        .size:           2
        .value_kind:     hidden_remainder_x
      - .offset:         60
        .size:           2
        .value_kind:     hidden_remainder_y
      - .offset:         62
        .size:           2
        .value_kind:     hidden_remainder_z
      - .offset:         80
        .size:           8
        .value_kind:     hidden_global_offset_x
      - .offset:         88
        .size:           8
        .value_kind:     hidden_global_offset_y
      - .offset:         96
        .size:           8
        .value_kind:     hidden_global_offset_z
      - .offset:         104
        .size:           2
        .value_kind:     hidden_grid_dims
      - .offset:         160
        .size:           4
        .value_kind:     hidden_dynamic_lds_size
    .group_segment_fixed_size: 0
    .kernarg_segment_align: 8
    .kernarg_segment_size: 296
    .language:       OpenCL C
    .language_version:
      - 2
      - 0
    .max_flat_workgroup_size: 512
    .name:           _Z11gemm_8phaseILi1EEvPKDF16_S1_PfPKfS4_
    .private_segment_fixed_size: 0
    .sgpr_count:     44
    .sgpr_spill_count: 0
    .symbol:         _Z11gemm_8phaseILi1EEvPKDF16_S1_PfPKfS4_.kd
    .uniform_work_group_size: 1
    .uses_dynamic_stack: false
    .vgpr_count:     256
    .vgpr_spill_count: 0
    .wavefront_size: 64
